# MoE phases: an XCD's 32 workgroups take 16 row tiles x 2 column tiles per round
# baseline (speedup 1.0000x reference)
; #define LAS __attribute__((address_space(3)))
;     __device__ __forceinline__ bool next(int i, Unit& u) const {
;         const int nm = c < nmain ? (nmain - c + G - 1) / G : 0;
;         int L; u.sub = -1;
;         if (i < nm) L = i * G + c;
;         else if (i == nm && tail > 0 && c / ways < tail) { L = nmain + c / ways; u.sub = ways == 4 ? (c & 3) : 4 + (c & 1); }
;         else return false;
;         const int rt = L >> 3; u.pm = rt; u.pn = rt_exp[rt] * 8 + (L & 7); return true; }
; __device__ __forceinline__ void ph_moe1(const Frame& F) {
;     LAS int* offs = (LAS int*)(F.lds + LDS_TAB); LAS int* cnts = offs + 128; LAS int* rt_exp = offs + 256;
;     expert_offsets(F, offs, cnts, rt_exp);
;     pg8::GroupedOrder So; So.init(rt_exp, (offs[64] >> 8) * 8, (int)gridDim.x, (int)blockIdx.x);
.LBB0_1008:
	v_writelane_b32 v248, s97, 60
	v_readlane_b32 s0, v248, 0
	v_readlane_b32 s1, v248, 1
	s_load_dword s74, s[0:1], 0xd0
	s_waitcnt lgkmcnt(0)
	s_cmpk_lg_u32 s74, 0x100
	s_cbranch_scc1 .Lmoe_noremap
	s_and_b32 s0, s97, 7
	s_lshr_b32 s1, s97, 3
	s_lshr_b32 s74, s0, 2
	s_lshl_b32 s74, s74, 4
	s_lshr_b32 s75, s1, 1
	s_add_i32 s74, s74, s75
	s_lshl_b32 s74, s74, 3
	s_and_b32 s0, s0, 3
	s_lshl_b32 s0, s0, 1
	s_and_b32 s1, s1, 1
	s_or_b32 s0, s0, s1
	s_or_b32 s97, s74, s0
